# v33_nopad
# baseline (speedup 1.0000x reference)
.LBB3_4:
	s_ashr_i32 s20, s3, 31
	s_mov_b32 s50, 0
	s_lshr_b32 s20, s20, 26
	s_add_i32 s20, s3, s20
	s_ashr_i32 s51, s50, 31
	s_ashr_i32 s94, s20, 6
	s_lshl_b64 s[56:57], s[50:51], 1
	s_add_u32 s20, s36, s56
	s_addc_u32 s21, s37, s57
	s_add_u32 s56, s30, s56
	s_addc_u32 s57, s31, s57
	v_lshl_add_u64 v[18:19], s[56:57], 0, v[108:109]
	v_add_co_u32_e32 v2, vcc, s35, v18
	s_nop 1
	v_addc_co_u32_e32 v3, vcc, 0, v19, vcc
	v_add_co_u32_e32 v4, vcc, s41, v18
	s_barrier
	s_nop 0
	v_addc_co_u32_e32 v5, vcc, 0, v19, vcc
	global_load_dwordx4 v[22:25], v106, s[56:57]
	global_load_dwordx4 v[26:29], v[2:3], off offset:1024
	global_load_dwordx4 v[30:33], v[4:5], off offset:2048
	v_add_co_u32_e32 v2, vcc, s43, v18
	s_mul_i32 s95, s94, 0x50
	s_nop 0
	v_addc_co_u32_e32 v3, vcc, 0, v19, vcc
	v_add_co_u32_e32 v4, vcc, s45, v18
	v_add_u32_e32 v42, s95, v1
	s_nop 0
	v_addc_co_u32_e32 v5, vcc, 0, v19, vcc
	global_load_dwordx4 v[34:37], v[2:3], off offset:3072
	global_load_dwordx4 v[38:41], v[4:5], off
	v_add_co_u32_e32 v2, vcc, s47, v18
	s_mul_i32 s58, s94, 0xffe9a800
	s_nop 0
	v_addc_co_u32_e32 v3, vcc, 0, v19, vcc
	v_add_co_u32_e32 v6, vcc, s33, v18
	v_max_i32_e32 v42, 3, v42
	s_nop 0
	v_addc_co_u32_e32 v7, vcc, 0, v19, vcc
	s_add_i32 s58, s58, s29
	v_add_co_u32_e32 v10, vcc, s49, v18
	v_add_u32_e32 v42, -3, v42
	v_add_u32_e32 v44, s95, v112
	v_addc_co_u32_e32 v11, vcc, 0, v19, vcc
	v_min_u32_e32 v66, 0x400, v42
	v_add_u32_e32 v42, s58, v133
	v_max_i32_e32 v44, 3, v44
	v_add_co_u32_e32 v14, vcc, s60, v18
	v_ashrrev_i32_e32 v43, 31, v42
	v_add_u32_e32 v44, -3, v44
	v_addc_co_u32_e32 v15, vcc, 0, v19, vcc
	v_lshl_add_u64 v[42:43], v[66:67], 0, v[42:43]
	v_min_u32_e32 v66, 0x400, v44
	v_add_u32_e32 v44, s58, v132
	v_add_co_u32_e32 v18, vcc, s61, v18
	v_ashrrev_i32_e32 v45, 31, v44
	s_nop 0
	v_addc_co_u32_e32 v19, vcc, 0, v19, vcc
	v_lshl_add_u64 v[42:43], v[42:43], 4, s[20:21]
	v_lshl_add_u64 v[44:45], v[66:67], 0, v[44:45]
	global_load_dwordx4 v[2:5], v[2:3], off offset:1024
	s_nop 0
	global_load_dwordx4 v[6:9], v[6:7], off offset:2048
	s_nop 0
	global_load_dwordx4 v[10:13], v[10:11], off offset:3072
	s_nop 0
	global_load_dwordx4 v[14:17], v[14:15], off
	v_lshl_add_u64 v[44:45], v[44:45], 4, s[20:21]
	global_load_dwordx4 v[18:21], v[18:19], off offset:1024
	s_nop 0
	global_load_dwordx4 v[62:65], v[42:43], off
	global_load_dwordx4 v[58:61], v[44:45], off
	v_add_u32_e32 v42, s95, v113
	v_max_i32_e32 v42, 3, v42
	v_add_u32_e32 v42, -3, v42
	v_add_u32_e32 v44, s95, v114
	v_min_u32_e32 v66, 0x400, v42
	v_add_u32_e32 v42, s58, v131
	v_max_i32_e32 v44, 3, v44
	v_ashrrev_i32_e32 v43, 31, v42
	v_add_u32_e32 v44, -3, v44
	v_lshl_add_u64 v[42:43], v[66:67], 0, v[42:43]
	v_min_u32_e32 v66, 0x400, v44
	v_add_u32_e32 v44, s58, v130
	v_ashrrev_i32_e32 v45, 31, v44
	v_lshl_add_u64 v[42:43], v[42:43], 4, s[20:21]
	v_lshl_add_u64 v[44:45], v[66:67], 0, v[44:45]
	v_lshl_add_u64 v[44:45], v[44:45], 4, s[20:21]
	global_load_dwordx4 v[54:57], v[42:43], off
	global_load_dwordx4 v[50:53], v[44:45], off
	v_add_u32_e32 v42, s95, v115
	v_max_i32_e32 v42, 3, v42
	v_add_u32_e32 v42, -3, v42
	v_add_u32_e32 v44, s95, v116
	v_min_u32_e32 v66, 0x400, v42
	v_add_u32_e32 v42, s58, v105
	v_max_i32_e32 v44, 3, v44
	v_ashrrev_i32_e32 v43, 31, v42
	v_add_u32_e32 v44, -3, v44
	v_lshl_add_u64 v[42:43], v[66:67], 0, v[42:43]
	v_min_u32_e32 v66, 0x400, v44
	v_add_u32_e32 v44, s58, v99
	v_ashrrev_i32_e32 v45, 31, v44
	v_lshl_add_u64 v[44:45], v[66:67], 0, v[44:45]
	v_lshl_add_u64 v[42:43], v[42:43], 4, s[20:21]
	v_lshl_add_u64 v[44:45], v[44:45], 4, s[20:21]
	global_load_dwordx4 v[46:49], v[42:43], off
	s_nop 0
	global_load_dwordx4 v[42:45], v[44:45], off
	s_cmp_gt_i32 s3, 63
	s_cbranch_scc0 .LBB3_22
	s_branch .Lmy_k2_gelu

.Lmy_k2_gelu:
	ds_read_b128 v[152:155], v69 offset:62400
	ds_read_b128 v[156:159], v69 offset:63104
	s_waitcnt vmcnt(5)
	v_cvt_f32_f16_sdwa v111, v62 dst_sel:DWORD dst_unused:UNUSED_PAD src0_sel:WORD_1
	v_cvt_f32_f16_e32 v110, v62
	s_add_i32 s58, s95, -3
	v_add_u32_e32 v66, s58, v1
	v_cmp_gt_u32_e32 vcc, s73, v66
	s_waitcnt lgkmcnt(0)
	v_pk_fma_f32 v[110:111], v[110:111], v[152:153], v[156:157]
	ds_read_b128 v[160:163], v69 offset:62416
	ds_read_b128 v[164:167], v69 offset:63120
	v_pk_mul_f32 v[152:153], v[110:111], s[28:29] op_sel_hi:[1,0]
	v_pk_mul_f32 v[170:171], v[110:111], 0.5 op_sel_hi:[1,0]
	v_fma_f32 v62, |v152|, s74, 1.0
	v_fma_f32 v107, |v153|, s74, 1.0
	v_rcp_f32_e32 v156, v62
	v_rcp_f32_e32 v157, v107
	v_mul_f32_e64 v62, |v152|, -|v152|
	v_mul_f32_e32 v62, 0x3fb8aa3b, v62
	v_exp_f32_e32 v168, v62
	v_mov_b64_e32 v[110:111], s[34:35]
	v_mul_f32_e64 v62, |v153|, -|v153|
	v_pk_fma_f32 v[172:173], v[156:157], s[40:41], v[110:111] op_sel_hi:[1,0,0]
	v_mul_f32_e32 v62, 0x3fb8aa3b, v62
	v_pk_fma_f32 v[172:173], v[156:157], v[172:173], s[42:43] op_sel_hi:[1,1,0]
	v_exp_f32_e32 v169, v62
	v_pk_fma_f32 v[172:173], v[156:157], v[172:173], s[44:45] op_sel_hi:[1,1,0]
	v_cndmask_b32_e64 v66, 0, 1.0, vcc
	v_pk_fma_f32 v[172:173], v[156:157], v[172:173], s[46:47] op_sel_hi:[1,1,0]
	s_nop 0
	v_pk_mul_f32 v[156:157], v[172:173], v[156:157] neg_lo:[0,1] neg_hi:[0,1]
	s_nop 0
	v_pk_fma_f32 v[156:157], v[156:157], v[168:169], 1.0 op_sel_hi:[1,1,0]
	s_nop 0
	v_bfi_b32 v153, s71, v157, v153
	v_bfi_b32 v152, s71, v156, v152
	v_cvt_f32_f16_sdwa v157, v63 dst_sel:DWORD dst_unused:UNUSED_PAD src0_sel:WORD_1
	v_cvt_f32_f16_e32 v156, v63
	v_pk_add_f32 v[152:153], v[152:153], 1.0 op_sel_hi:[1,0]
	s_nop 0
	v_pk_mul_f32 v[62:63], v[170:171], v[152:153]
	v_pk_fma_f32 v[152:153], v[156:157], v[154:155], v[158:159]
	v_pk_mul_f32 v[62:63], v[66:67], v[62:63] op_sel_hi:[0,1]
	v_pk_mul_f32 v[154:155], v[152:153], s[28:29] op_sel_hi:[1,0]
	v_cvt_pk_f16_f32 v62, v62, v63
	v_fma_f32 v63, |v154|, s74, 1.0
	v_fma_f32 v107, |v155|, s74, 1.0
	v_rcp_f32_e32 v156, v63
	v_rcp_f32_e32 v157, v107
	v_mul_f32_e64 v63, |v154|, -|v154|
	v_mul_f32_e32 v63, 0x3fb8aa3b, v63
	v_exp_f32_e32 v158, v63
	v_mul_f32_e64 v63, |v155|, -|v155|
	v_pk_fma_f32 v[168:169], v[156:157], s[40:41], v[110:111] op_sel_hi:[1,0,0]
	v_mul_f32_e32 v63, 0x3fb8aa3b, v63
	v_pk_fma_f32 v[168:169], v[156:157], v[168:169], s[42:43] op_sel_hi:[1,1,0]
	v_exp_f32_e32 v159, v63
	v_pk_fma_f32 v[168:169], v[156:157], v[168:169], s[44:45] op_sel_hi:[1,1,0]
	v_pk_mul_f32 v[152:153], v[152:153], 0.5 op_sel_hi:[1,0]
	v_pk_fma_f32 v[168:169], v[156:157], v[168:169], s[46:47] op_sel_hi:[1,1,0]
	s_nop 0
	v_pk_mul_f32 v[156:157], v[168:169], v[156:157] neg_lo:[0,1] neg_hi:[0,1]
	s_nop 0
	v_pk_fma_f32 v[156:157], v[156:157], v[158:159], 1.0 op_sel_hi:[1,1,0]
	s_nop 0
	v_bfi_b32 v155, s71, v157, v155
	v_bfi_b32 v154, s71, v156, v154
	v_cvt_f32_f16_sdwa v157, v64 dst_sel:DWORD dst_unused:UNUSED_PAD src0_sel:WORD_1
	v_cvt_f32_f16_e32 v156, v64
	v_pk_add_f32 v[154:155], v[154:155], 1.0 op_sel_hi:[1,0]
	s_nop 0
	v_pk_mul_f32 v[152:153], v[152:153], v[154:155]
	s_nop 0
	v_pk_mul_f32 v[152:153], v[66:67], v[152:153] op_sel_hi:[0,1]
	v_cvt_pk_f16_f32 v63, v152, v153
	s_waitcnt lgkmcnt(0)
	v_pk_fma_f32 v[152:153], v[156:157], v[160:161], v[164:165]
	s_waitcnt vmcnt(4)
	v_cvt_f32_f16_sdwa v165, v58 dst_sel:DWORD dst_unused:UNUSED_PAD src0_sel:WORD_1
	v_pk_mul_f32 v[154:155], v[152:153], s[28:29] op_sel_hi:[1,0]
	v_pk_mul_f32 v[152:153], v[152:153], 0.5 op_sel_hi:[1,0]
	v_fma_f32 v64, |v154|, s74, 1.0
	v_fma_f32 v107, |v155|, s74, 1.0
	v_rcp_f32_e32 v156, v64
	v_rcp_f32_e32 v157, v107
	v_mul_f32_e64 v64, |v154|, -|v154|
	v_mul_f32_e32 v64, 0x3fb8aa3b, v64
	v_exp_f32_e32 v158, v64
	v_mul_f32_e64 v64, |v155|, -|v155|
	v_pk_fma_f32 v[160:161], v[156:157], s[40:41], v[110:111] op_sel_hi:[1,0,0]
	v_mul_f32_e32 v64, 0x3fb8aa3b, v64
	v_pk_fma_f32 v[160:161], v[156:157], v[160:161], s[42:43] op_sel_hi:[1,1,0]
	v_exp_f32_e32 v159, v64
	v_pk_fma_f32 v[160:161], v[156:157], v[160:161], s[44:45] op_sel_hi:[1,1,0]
	v_cvt_f32_f16_e32 v164, v58
	v_pk_fma_f32 v[160:161], v[156:157], v[160:161], s[46:47] op_sel_hi:[1,1,0]
	s_nop 0
	v_pk_mul_f32 v[156:157], v[160:161], v[156:157] neg_lo:[0,1] neg_hi:[0,1]
	s_nop 0
	v_pk_fma_f32 v[156:157], v[156:157], v[158:159], 1.0 op_sel_hi:[1,1,0]
	s_nop 0
	v_bfi_b32 v155, s71, v157, v155
	v_bfi_b32 v154, s71, v156, v154
	v_cvt_f32_f16_sdwa v157, v65 dst_sel:DWORD dst_unused:UNUSED_PAD src0_sel:WORD_1
	v_cvt_f32_f16_e32 v156, v65
	v_pk_add_f32 v[154:155], v[154:155], 1.0 op_sel_hi:[1,0]
	s_nop 0
	v_pk_mul_f32 v[64:65], v[152:153], v[154:155]
	v_pk_fma_f32 v[152:153], v[156:157], v[162:163], v[166:167]
	v_pk_mul_f32 v[64:65], v[66:67], v[64:65] op_sel_hi:[0,1]
	v_pk_mul_f32 v[154:155], v[152:153], s[28:29] op_sel_hi:[1,0]
	v_cvt_pk_f16_f32 v64, v64, v65
	v_fma_f32 v65, |v154|, s74, 1.0
	v_fma_f32 v107, |v155|, s74, 1.0
	v_rcp_f32_e32 v156, v65
	v_rcp_f32_e32 v157, v107
	v_mul_f32_e64 v65, |v154|, -|v154|
	v_mul_f32_e32 v65, 0x3fb8aa3b, v65
	v_exp_f32_e32 v158, v65
	v_mul_f32_e64 v65, |v155|, -|v155|
	v_pk_fma_f32 v[160:161], v[156:157], s[40:41], v[110:111] op_sel_hi:[1,0,0]
	v_mul_f32_e32 v65, 0x3fb8aa3b, v65
	v_pk_fma_f32 v[160:161], v[156:157], v[160:161], s[42:43] op_sel_hi:[1,1,0]
	v_exp_f32_e32 v159, v65
	v_pk_fma_f32 v[160:161], v[156:157], v[160:161], s[44:45] op_sel_hi:[1,1,0]
	v_pk_mul_f32 v[152:153], v[152:153], 0.5 op_sel_hi:[1,0]
	v_pk_fma_f32 v[160:161], v[156:157], v[160:161], s[46:47] op_sel_hi:[1,1,0]
	s_nop 0
	v_pk_mul_f32 v[156:157], v[160:161], v[156:157] neg_lo:[0,1] neg_hi:[0,1]
	s_nop 0
	v_pk_fma_f32 v[156:157], v[156:157], v[158:159], 1.0 op_sel_hi:[1,1,0]
	s_nop 0
	v_bfi_b32 v155, s71, v157, v155
	v_bfi_b32 v154, s71, v156, v154
	v_pk_add_f32 v[154:155], v[154:155], 1.0 op_sel_hi:[1,0]
	s_nop 0
	v_pk_mul_f32 v[152:153], v[152:153], v[154:155]
	s_nop 0
	v_pk_mul_f32 v[152:153], v[66:67], v[152:153] op_sel_hi:[0,1]
	v_cvt_pk_f16_f32 v65, v152, v153
	ds_write_b128 v138, v[62:65]
	ds_read_b128 v[62:65], v118 offset:62400
	ds_read_b128 v[152:155], v118 offset:63104
	v_add_u32_e32 v66, s58, v112
	v_cmp_gt_u32_e32 vcc, s73, v66
	ds_read_b128 v[156:159], v118 offset:62416
	ds_read_b128 v[160:163], v118 offset:63120
	v_cndmask_b32_e64 v66, 0, 1.0, vcc
	s_waitcnt lgkmcnt(2)
	v_pk_fma_f32 v[62:63], v[164:165], v[62:63], v[152:153]
	s_nop 0
	v_pk_mul_f32 v[152:153], v[62:63], s[28:29] op_sel_hi:[1,0]
	v_pk_mul_f32 v[62:63], v[62:63], 0.5 op_sel_hi:[1,0]
	v_fma_f32 v58, |v152|, s74, 1.0
	v_fma_f32 v107, |v153|, s74, 1.0
	v_rcp_f32_e32 v164, v58
	v_rcp_f32_e32 v165, v107
	v_mul_f32_e64 v58, |v152|, -|v152|
	v_mul_f32_e32 v58, 0x3fb8aa3b, v58
	v_exp_f32_e32 v166, v58
	v_mul_f32_e64 v58, |v153|, -|v153|
	v_pk_fma_f32 v[168:169], v[164:165], s[40:41], v[110:111] op_sel_hi:[1,0,0]
	v_mul_f32_e32 v58, 0x3fb8aa3b, v58
	v_pk_fma_f32 v[168:169], v[164:165], v[168:169], s[42:43] op_sel_hi:[1,1,0]
	v_exp_f32_e32 v167, v58
	v_pk_fma_f32 v[168:169], v[164:165], v[168:169], s[44:45] op_sel_hi:[1,1,0]
	s_nop 0
	v_pk_fma_f32 v[168:169], v[164:165], v[168:169], s[46:47] op_sel_hi:[1,1,0]
	s_nop 0
	v_pk_mul_f32 v[164:165], v[168:169], v[164:165] neg_lo:[0,1] neg_hi:[0,1]
	s_nop 0
	v_pk_fma_f32 v[164:165], v[164:165], v[166:167], 1.0 op_sel_hi:[1,1,0]
	s_nop 0
	v_bfi_b32 v153, s71, v165, v153
	v_bfi_b32 v152, s71, v164, v152
	v_cvt_f32_f16_sdwa v165, v59 dst_sel:DWORD dst_unused:UNUSED_PAD src0_sel:WORD_1
	v_cvt_f32_f16_e32 v164, v59
	v_pk_add_f32 v[152:153], v[152:153], 1.0 op_sel_hi:[1,0]
	s_nop 0
	v_pk_mul_f32 v[58:59], v[62:63], v[152:153]
	v_pk_fma_f32 v[62:63], v[164:165], v[64:65], v[154:155]
	v_pk_mul_f32 v[58:59], v[66:67], v[58:59] op_sel_hi:[0,1]
	v_pk_mul_f32 v[64:65], v[62:63], s[28:29] op_sel_hi:[1,0]
	v_cvt_pk_f16_f32 v58, v58, v59
	v_fma_f32 v59, |v64|, s74, 1.0
	v_fma_f32 v107, |v65|, s74, 1.0
	v_rcp_f32_e32 v152, v59
	v_rcp_f32_e32 v153, v107
	v_mul_f32_e64 v59, |v64|, -|v64|
	v_mul_f32_e32 v59, 0x3fb8aa3b, v59
	v_exp_f32_e32 v154, v59
	v_mul_f32_e64 v59, |v65|, -|v65|
	v_pk_fma_f32 v[164:165], v[152:153], s[40:41], v[110:111] op_sel_hi:[1,0,0]
	v_mul_f32_e32 v59, 0x3fb8aa3b, v59
	v_pk_fma_f32 v[164:165], v[152:153], v[164:165], s[42:43] op_sel_hi:[1,1,0]
	v_exp_f32_e32 v155, v59
	v_pk_fma_f32 v[164:165], v[152:153], v[164:165], s[44:45] op_sel_hi:[1,1,0]
	v_pk_mul_f32 v[62:63], v[62:63], 0.5 op_sel_hi:[1,0]
	v_pk_fma_f32 v[164:165], v[152:153], v[164:165], s[46:47] op_sel_hi:[1,1,0]
	s_nop 0
	v_pk_mul_f32 v[152:153], v[164:165], v[152:153] neg_lo:[0,1] neg_hi:[0,1]
	s_nop 0
	v_pk_fma_f32 v[152:153], v[152:153], v[154:155], 1.0 op_sel_hi:[1,1,0]
	s_nop 0
	v_bfi_b32 v65, s71, v153, v65
	v_bfi_b32 v64, s71, v152, v64
	v_cvt_f32_f16_sdwa v153, v60 dst_sel:DWORD dst_unused:UNUSED_PAD src0_sel:WORD_1
	v_cvt_f32_f16_e32 v152, v60
	v_pk_add_f32 v[64:65], v[64:65], 1.0 op_sel_hi:[1,0]
	s_nop 0
	v_pk_mul_f32 v[62:63], v[62:63], v[64:65]
	s_nop 0
	v_pk_mul_f32 v[62:63], v[66:67], v[62:63] op_sel_hi:[0,1]
	v_cvt_pk_f16_f32 v59, v62, v63
	s_waitcnt lgkmcnt(0)
	v_pk_fma_f32 v[62:63], v[152:153], v[156:157], v[160:161]
	s_waitcnt vmcnt(3)
	v_cvt_f32_f16_sdwa v161, v54 dst_sel:DWORD dst_unused:UNUSED_PAD src0_sel:WORD_1
	v_pk_mul_f32 v[64:65], v[62:63], s[28:29] op_sel_hi:[1,0]
	v_pk_mul_f32 v[62:63], v[62:63], 0.5 op_sel_hi:[1,0]
	v_fma_f32 v60, |v64|, s74, 1.0
	v_fma_f32 v107, |v65|, s74, 1.0
	v_rcp_f32_e32 v152, v60
	v_rcp_f32_e32 v153, v107
	v_mul_f32_e64 v60, |v64|, -|v64|
	v_mul_f32_e32 v60, 0x3fb8aa3b, v60
	v_exp_f32_e32 v154, v60
	v_mul_f32_e64 v60, |v65|, -|v65|
	v_pk_fma_f32 v[156:157], v[152:153], s[40:41], v[110:111] op_sel_hi:[1,0,0]
	v_mul_f32_e32 v60, 0x3fb8aa3b, v60
	v_pk_fma_f32 v[156:157], v[152:153], v[156:157], s[42:43] op_sel_hi:[1,1,0]
	v_exp_f32_e32 v155, v60
	v_pk_fma_f32 v[156:157], v[152:153], v[156:157], s[44:45] op_sel_hi:[1,1,0]
	v_cvt_f32_f16_e32 v160, v54
	v_pk_fma_f32 v[156:157], v[152:153], v[156:157], s[46:47] op_sel_hi:[1,1,0]
	s_nop 0
	v_pk_mul_f32 v[152:153], v[156:157], v[152:153] neg_lo:[0,1] neg_hi:[0,1]
	s_nop 0
	v_pk_fma_f32 v[152:153], v[152:153], v[154:155], 1.0 op_sel_hi:[1,1,0]
	s_nop 0
	v_bfi_b32 v65, s71, v153, v65
	v_bfi_b32 v64, s71, v152, v64
	v_cvt_f32_f16_sdwa v153, v61 dst_sel:DWORD dst_unused:UNUSED_PAD src0_sel:WORD_1
	v_cvt_f32_f16_e32 v152, v61
	v_pk_add_f32 v[64:65], v[64:65], 1.0 op_sel_hi:[1,0]
	s_nop 0
	v_pk_mul_f32 v[60:61], v[62:63], v[64:65]
	v_pk_fma_f32 v[62:63], v[152:153], v[158:159], v[162:163]
	v_pk_mul_f32 v[60:61], v[66:67], v[60:61] op_sel_hi:[0,1]
	v_pk_mul_f32 v[64:65], v[62:63], s[28:29] op_sel_hi:[1,0]
	v_cvt_pk_f16_f32 v60, v60, v61
	v_fma_f32 v61, |v64|, s74, 1.0
	v_fma_f32 v107, |v65|, s74, 1.0
	v_rcp_f32_e32 v152, v61
	v_rcp_f32_e32 v153, v107
	v_mul_f32_e64 v61, |v64|, -|v64|
	v_mul_f32_e32 v61, 0x3fb8aa3b, v61
	v_exp_f32_e32 v154, v61
	v_mul_f32_e64 v61, |v65|, -|v65|
	v_pk_fma_f32 v[156:157], v[152:153], s[40:41], v[110:111] op_sel_hi:[1,0,0]
	v_mul_f32_e32 v61, 0x3fb8aa3b, v61
	v_pk_fma_f32 v[156:157], v[152:153], v[156:157], s[42:43] op_sel_hi:[1,1,0]
	v_exp_f32_e32 v155, v61
	v_pk_fma_f32 v[156:157], v[152:153], v[156:157], s[44:45] op_sel_hi:[1,1,0]
	v_pk_mul_f32 v[62:63], v[62:63], 0.5 op_sel_hi:[1,0]
	v_pk_fma_f32 v[156:157], v[152:153], v[156:157], s[46:47] op_sel_hi:[1,1,0]
	s_nop 0
	v_pk_mul_f32 v[152:153], v[156:157], v[152:153] neg_lo:[0,1] neg_hi:[0,1]
	s_nop 0
	v_pk_fma_f32 v[152:153], v[152:153], v[154:155], 1.0 op_sel_hi:[1,1,0]
	s_nop 0
	v_bfi_b32 v65, s71, v153, v65
	v_bfi_b32 v64, s71, v152, v64
	v_pk_add_f32 v[64:65], v[64:65], 1.0 op_sel_hi:[1,0]
	s_nop 0
	v_pk_mul_f32 v[62:63], v[62:63], v[64:65]
	s_nop 0
	v_pk_mul_f32 v[62:63], v[66:67], v[62:63] op_sel_hi:[0,1]
	v_cvt_pk_f16_f32 v61, v62, v63
	ds_write_b128 v139, v[58:61]
	ds_read_b128 v[58:61], v119 offset:62400
	ds_read_b128 v[62:65], v119 offset:63104
	v_add_u32_e32 v66, s58, v113
	v_cmp_gt_u32_e32 vcc, s73, v66
	ds_read_b128 v[152:155], v119 offset:62416
	ds_read_b128 v[156:159], v119 offset:63120
	v_cndmask_b32_e64 v66, 0, 1.0, vcc
	s_waitcnt lgkmcnt(2)
	v_pk_fma_f32 v[58:59], v[160:161], v[58:59], v[62:63]
	s_nop 0
	v_pk_mul_f32 v[62:63], v[58:59], s[28:29] op_sel_hi:[1,0]
	v_pk_mul_f32 v[58:59], v[58:59], 0.5 op_sel_hi:[1,0]
	v_fma_f32 v54, |v62|, s74, 1.0
	v_fma_f32 v107, |v63|, s74, 1.0
	v_rcp_f32_e32 v160, v54
	v_rcp_f32_e32 v161, v107
	v_mul_f32_e64 v54, |v62|, -|v62|
	v_mul_f32_e32 v54, 0x3fb8aa3b, v54
	v_exp_f32_e32 v162, v54
	v_mul_f32_e64 v54, |v63|, -|v63|
	v_pk_fma_f32 v[164:165], v[160:161], s[40:41], v[110:111] op_sel_hi:[1,0,0]
	v_mul_f32_e32 v54, 0x3fb8aa3b, v54
	v_pk_fma_f32 v[164:165], v[160:161], v[164:165], s[42:43] op_sel_hi:[1,1,0]
	v_exp_f32_e32 v163, v54
	v_pk_fma_f32 v[164:165], v[160:161], v[164:165], s[44:45] op_sel_hi:[1,1,0]
	s_nop 0
	v_pk_fma_f32 v[164:165], v[160:161], v[164:165], s[46:47] op_sel_hi:[1,1,0]
	s_nop 0
	v_pk_mul_f32 v[160:161], v[164:165], v[160:161] neg_lo:[0,1] neg_hi:[0,1]
	s_nop 0
	v_pk_fma_f32 v[160:161], v[160:161], v[162:163], 1.0 op_sel_hi:[1,1,0]
	s_nop 0
	v_bfi_b32 v63, s71, v161, v63
	v_bfi_b32 v62, s71, v160, v62
	v_cvt_f32_f16_sdwa v161, v55 dst_sel:DWORD dst_unused:UNUSED_PAD src0_sel:WORD_1
	v_cvt_f32_f16_e32 v160, v55
	v_pk_add_f32 v[62:63], v[62:63], 1.0 op_sel_hi:[1,0]
	s_nop 0
	v_pk_mul_f32 v[54:55], v[58:59], v[62:63]
	v_pk_fma_f32 v[58:59], v[160:161], v[60:61], v[64:65]
	v_pk_mul_f32 v[54:55], v[66:67], v[54:55] op_sel_hi:[0,1]
	v_pk_mul_f32 v[60:61], v[58:59], s[28:29] op_sel_hi:[1,0]
	v_cvt_pk_f16_f32 v54, v54, v55
	v_fma_f32 v55, |v60|, s74, 1.0
	v_fma_f32 v63, |v61|, s74, 1.0
	v_rcp_f32_e32 v62, v55
	v_rcp_f32_e32 v63, v63
	v_mul_f32_e64 v55, |v60|, -|v60|
	v_mul_f32_e32 v55, 0x3fb8aa3b, v55
	v_exp_f32_e32 v64, v55
	v_mul_f32_e64 v55, |v61|, -|v61|
	v_pk_fma_f32 v[160:161], v[62:63], s[40:41], v[110:111] op_sel_hi:[1,0,0]
	v_mul_f32_e32 v55, 0x3fb8aa3b, v55
	v_pk_fma_f32 v[160:161], v[62:63], v[160:161], s[42:43] op_sel_hi:[1,1,0]
	v_exp_f32_e32 v65, v55
	v_pk_fma_f32 v[160:161], v[62:63], v[160:161], s[44:45] op_sel_hi:[1,1,0]
	v_pk_mul_f32 v[58:59], v[58:59], 0.5 op_sel_hi:[1,0]
	v_pk_fma_f32 v[160:161], v[62:63], v[160:161], s[46:47] op_sel_hi:[1,1,0]
	s_nop 0
	v_pk_mul_f32 v[62:63], v[160:161], v[62:63] neg_lo:[0,1] neg_hi:[0,1]
	s_nop 0
	v_pk_fma_f32 v[62:63], v[62:63], v[64:65], 1.0 op_sel_hi:[1,1,0]
	s_nop 0
	v_bfi_b32 v61, s71, v63, v61
	v_bfi_b32 v60, s71, v62, v60
	v_cvt_f32_f16_sdwa v63, v56 dst_sel:DWORD dst_unused:UNUSED_PAD src0_sel:WORD_1
	v_cvt_f32_f16_e32 v62, v56
	v_pk_add_f32 v[60:61], v[60:61], 1.0 op_sel_hi:[1,0]
	s_nop 0
	v_pk_mul_f32 v[58:59], v[58:59], v[60:61]
	s_nop 0
	v_pk_mul_f32 v[58:59], v[66:67], v[58:59] op_sel_hi:[0,1]
	v_cvt_pk_f16_f32 v55, v58, v59
	s_waitcnt lgkmcnt(0)
	v_pk_fma_f32 v[58:59], v[62:63], v[152:153], v[156:157]
	s_nop 0
	v_pk_mul_f32 v[60:61], v[58:59], s[28:29] op_sel_hi:[1,0]
	v_pk_mul_f32 v[58:59], v[58:59], 0.5 op_sel_hi:[1,0]
	v_fma_f32 v56, |v60|, s74, 1.0
	v_fma_f32 v63, |v61|, s74, 1.0
	v_rcp_f32_e32 v62, v56
	v_rcp_f32_e32 v63, v63
	v_mul_f32_e64 v56, |v60|, -|v60|
	v_mul_f32_e32 v56, 0x3fb8aa3b, v56
	v_exp_f32_e32 v64, v56
	v_mul_f32_e64 v56, |v61|, -|v61|
	v_pk_fma_f32 v[152:153], v[62:63], s[40:41], v[110:111] op_sel_hi:[1,0,0]
	v_mul_f32_e32 v56, 0x3fb8aa3b, v56
	v_pk_fma_f32 v[152:153], v[62:63], v[152:153], s[42:43] op_sel_hi:[1,1,0]
	v_exp_f32_e32 v65, v56
	v_pk_fma_f32 v[152:153], v[62:63], v[152:153], s[44:45] op_sel_hi:[1,1,0]
	s_nop 0
	v_pk_fma_f32 v[152:153], v[62:63], v[152:153], s[46:47] op_sel_hi:[1,1,0]
	s_nop 0
	v_pk_mul_f32 v[62:63], v[152:153], v[62:63] neg_lo:[0,1] neg_hi:[0,1]
	s_nop 0
	v_pk_fma_f32 v[62:63], v[62:63], v[64:65], 1.0 op_sel_hi:[1,1,0]
	s_nop 0
	v_bfi_b32 v61, s71, v63, v61
	v_bfi_b32 v60, s71, v62, v60
	v_cvt_f32_f16_sdwa v63, v57 dst_sel:DWORD dst_unused:UNUSED_PAD src0_sel:WORD_1
	v_cvt_f32_f16_e32 v62, v57
	v_pk_add_f32 v[60:61], v[60:61], 1.0 op_sel_hi:[1,0]
	s_nop 0
	v_pk_mul_f32 v[56:57], v[58:59], v[60:61]
	v_pk_fma_f32 v[58:59], v[62:63], v[154:155], v[158:159]
	v_pk_mul_f32 v[56:57], v[66:67], v[56:57] op_sel_hi:[0,1]
	v_pk_mul_f32 v[60:61], v[58:59], s[28:29] op_sel_hi:[1,0]
	v_cvt_pk_f16_f32 v56, v56, v57
	v_fma_f32 v57, |v60|, s74, 1.0
	v_fma_f32 v63, |v61|, s74, 1.0
	v_rcp_f32_e32 v62, v57
	v_rcp_f32_e32 v63, v63
	v_mul_f32_e64 v57, |v60|, -|v60|
	v_mul_f32_e32 v57, 0x3fb8aa3b, v57
	v_exp_f32_e32 v64, v57
	v_mul_f32_e64 v57, |v61|, -|v61|
	v_pk_fma_f32 v[110:111], v[62:63], s[40:41], v[110:111] op_sel_hi:[1,0,0]
	v_mul_f32_e32 v57, 0x3fb8aa3b, v57
	v_pk_fma_f32 v[110:111], v[62:63], v[110:111], s[42:43] op_sel_hi:[1,1,0]
	v_exp_f32_e32 v65, v57
	v_pk_fma_f32 v[110:111], v[62:63], v[110:111], s[44:45] op_sel_hi:[1,1,0]
	v_pk_mul_f32 v[58:59], v[58:59], 0.5 op_sel_hi:[1,0]
	v_pk_fma_f32 v[110:111], v[62:63], v[110:111], s[46:47] op_sel_hi:[1,1,0]
	s_nop 0
	v_pk_mul_f32 v[62:63], v[110:111], v[62:63] neg_lo:[0,1] neg_hi:[0,1]
	s_nop 0
	v_pk_fma_f32 v[62:63], v[62:63], v[64:65], 1.0 op_sel_hi:[1,1,0]
	s_nop 0
	v_bfi_b32 v61, s71, v63, v61
	v_bfi_b32 v60, s71, v62, v60
	v_pk_add_f32 v[60:61], v[60:61], 1.0 op_sel_hi:[1,0]
	s_nop 0
	v_pk_mul_f32 v[58:59], v[58:59], v[60:61]
	s_nop 0
	v_pk_mul_f32 v[58:59], v[66:67], v[58:59] op_sel_hi:[0,1]
	v_cvt_pk_f16_f32 v57, v58, v59
	ds_write_b128 v140, v[54:57]
	s_and_saveexec_b64 s[20:21], s[12:13]
	s_cbranch_execnz .LBB3_36
	s_or_b64 exec, exec, s[20:21]
	s_and_saveexec_b64 s[20:21], s[14:15]
	s_cbranch_execnz .LBB3_37
